# layer-1 w_down conversion split moved: 1536 items under the scan R2 phase, 9728 under layer 1's top-k
# baseline (speedup 1.0000x reference)
.LBB0_1916:
	s_or_b64 exec, exec, s[0:1]
	s_movk_i32 s0, 0x600
	v_cmp_gt_i32_e32 vcc, s0, v24
	s_and_saveexec_b64 s[0:1], vcc
	s_cbranch_execz .LBB0_1919
	s_add_u32 s4, s48, 0x50000000
	s_addc_u32 s5, s49, 0
	s_mov_b64 s[6:7], 0
	s_mov_b32 s9, 0x2e8ba2e9
	s_mov_b32 s10, 0xb00000
	v_mov_b64_e32 v[22:23], s[74:75]
	v_mov_b32_e32 v21, 0
	v_add_u32_e32 v31, 0x410, v26
	v_add_u32_e32 v32, 0x418, v26
	v_add_u32_e32 v33, 0x820, v26
	v_add_u32_e32 v34, 0x828, v26
	v_add_u32_e32 v35, 0xc30, v26
	v_add_u32_e32 v36, 0xc38, v26
	v_add_u32_e32 v37, 0x1040, v26
	v_add_u32_e32 v38, 0x1048, v26
	v_add_u32_e32 v39, 0x1450, v26
	v_add_u32_e32 v40, 0x1458, v26
	v_add_u32_e32 v41, 0x1860, v26
	v_add_u32_e32 v42, 0x1868, v26
	v_add_u32_e32 v43, 0x1c70, v26
	v_add_u32_e32 v44, 0x1c78, v26
	v_add_u32_e32 v45, 0x2080, v26
	v_add_u32_e32 v46, 0x2088, v26
	v_add_u32_e32 v47, 0x2490, v26
	v_add_u32_e32 v48, 0x2498, v26
	v_add_u32_e32 v49, 0x28a0, v26
	v_add_u32_e32 v50, 0x28a8, v26
	v_add_u32_e32 v51, 0x2cb0, v26
	v_add_u32_e32 v52, 0x2cb8, v26
	v_add_u32_e32 v53, 0x30c0, v26
	v_add_u32_e32 v54, 0x30c8, v26
	v_add_u32_e32 v55, 0x34d0, v26
	v_add_u32_e32 v56, 0x34d8, v26
	v_add_u32_e32 v57, 0x38e0, v26
	v_add_u32_e32 v58, 0x38e8, v26
	v_add_u32_e32 v59, 0x3cf0, v26
	v_add_u32_e32 v60, 0x3cf8, v26
	s_mov_b32 s11, 0xc3e00000
	v_mov_b32_e32 v61, 0x43e00000
	s_movk_i32 s12, 0x5ff
	v_mov_b32_e32 v62, 6
	v_add_u32_e32 v63, 0x400, v1
	v_add_u32_e32 v64, 0x800, v1
	v_add_u32_e32 v65, 0xc00, v1

.LBB0_2375:
	s_cmp_gt_i32 s50, 19
	s_cselect_b64 s[0:1], -1, 0
	s_cmp_lt_i32 s51, 20
	s_cselect_b64 s[2:3], -1, 0
	s_or_b64 s[2:3], s[0:1], s[2:3]
	s_and_b64 vcc, exec, s[2:3]
	s_cbranch_vccnz .LBB0_2592
	v_readlane_b32 s0, v253, 0
	v_readlane_b32 s1, v253, 1
	s_mov_b32 s4, s0
	s_cmp_lt_i32 s0, 32
	s_cselect_b64 s[0:1], -1, 0
	s_cmp_gt_i32 s4, 31
	v_readlane_b32 s6, v253, 63
	s_waitcnt vmcnt(0)
	v_ashrrev_i32_e32 v25, 6, v138
	s_cselect_b64 s[4:5], -1, 0
	s_addk_i32 s6, 0xff00
	v_add_u32_e32 v1, s6, v25
	s_movk_i32 s6, 0x2600
	v_cmp_gt_i32_e32 vcc, s6, v1
	v_and_b32_e32 v24, 63, v138
	s_and_b64 s[6:7], s[4:5], vcc
	s_and_saveexec_b64 s[4:5], s[6:7]
	s_cbranch_execz .LBB0_2379
	s_movk_i32 s6, 0x4200
	v_mul_lo_u32 v2, v25, s6
	s_waitcnt lgkmcnt(0)
	v_add_u32_e32 v3, 0, v2
	v_lshlrev_b32_e32 v2, 2, v24
	v_lshlrev_b32_e32 v6, 4, v24
	v_lshrrev_b32_e32 v26, 4, v24
	v_and_b32_e32 v2, 60, v2
	v_and_b32_e32 v18, 48, v6
	s_add_i32 s10, s70, 0xffffff00
	v_lshl_add_u32 v4, v2, 2, v3
	v_mul_u32_u24_e32 v5, 0x104, v26
	v_mul_u32_u24_e32 v6, 0x104, v18
	v_and_b32_e32 v7, 60, v24
	s_add_u32 s6, s48, 0x50000000
	v_mov_b32_e32 v19, 0
	v_lshrrev_b32_e32 v27, 2, v24
	v_add3_u32 v28, v3, v6, v7
	v_add_u32_e32 v32, v4, v5
	s_addc_u32 s7, s49, 0
	v_or_b32_e32 v29, 16, v27
	v_or_b32_e32 v30, 32, v27
	v_or_b32_e32 v31, 48, v27
	s_mov_b64 s[8:9], 0
	s_mov_b32 s11, 0x2e8ba2e9
	s_mov_b32 s12, 0xb00000
	v_mov_b64_e32 v[20:21], s[74:75]
	v_lshlrev_b32_e32 v22, 2, v2
	v_mov_b32_e32 v23, v19
	v_add_u32_e32 v33, 0x410, v32
	v_add_u32_e32 v34, 0x418, v32
	v_add_u32_e32 v35, 0x820, v32
	v_add_u32_e32 v36, 0x828, v32
	v_add_u32_e32 v37, 0xc30, v32
	v_add_u32_e32 v38, 0xc38, v32
	v_add_u32_e32 v39, 0x1040, v32
	v_add_u32_e32 v40, 0x1048, v32
	v_add_u32_e32 v41, 0x1450, v32
	v_add_u32_e32 v42, 0x1458, v32
	v_add_u32_e32 v43, 0x1860, v32
	v_add_u32_e32 v44, 0x1868, v32
	v_add_u32_e32 v45, 0x1c70, v32
	v_add_u32_e32 v46, 0x1c78, v32
	v_add_u32_e32 v47, 0x2080, v32
	v_add_u32_e32 v48, 0x2088, v32
	v_add_u32_e32 v49, 0x2490, v32
	v_add_u32_e32 v50, 0x2498, v32
	v_add_u32_e32 v51, 0x28a0, v32
	v_add_u32_e32 v52, 0x28a8, v32
	v_add_u32_e32 v53, 0x2cb0, v32
	v_add_u32_e32 v54, 0x2cb8, v32
	v_add_u32_e32 v55, 0x30c0, v32
	v_add_u32_e32 v56, 0x30c8, v32
	v_add_u32_e32 v57, 0x34d0, v32
	v_add_u32_e32 v58, 0x34d8, v32
	v_add_u32_e32 v59, 0x38e0, v32
	v_add_u32_e32 v60, 0x38e8, v32
	v_add_u32_e32 v61, 0x3cf0, v32
	v_add_u32_e32 v62, 0x3cf8, v32
	s_mov_b32 s13, 0xc3e00000
	v_mov_b32_e32 v63, 0x43e00000
	s_movk_i32 s14, 0x25ff
	v_mov_b32_e32 v64, 6
	v_add_u32_e32 v65, 0x400, v28
	v_add_u32_e32 v66, 0x800, v28
	v_add_u32_e32 v67, 0xc00, v28
.LBB0_2378:
	v_add_u32_e32 v70, 0x600, v1
	v_mul_hi_i32 v68, v70, s11
	v_lshrrev_b32_e32 v69, 31, v68
	v_ashrrev_i32_e32 v68, 7, v68
	v_add_u32_e32 v68, v68, v69
	v_mul_i32_i24_e32 v72, 0x2c0, v68
	v_sub_u32_e32 v72, v70, v72
	v_ashrrev_i16_e32 v73, 15, v72
	v_lshrrev_b16_e32 v73, 12, v73
	v_add_u16_e32 v73, v72, v73
	v_ashrrev_i16_e32 v74, 4, v73
	v_and_b32_e32 v73, -16, v73
	v_sub_u16_e32 v73, v72, v73
	v_lshlrev_b32_sdwa v72, v64, sext(v74) dst_sel:DWORD dst_unused:UNUSED_PAD src0_sel:DWORD src1_sel:WORD_0
	v_add_u32_e32 v71, 16, v68
	v_lshlrev_b32_sdwa v74, v64, sext(v73) dst_sel:DWORD dst_unused:UNUSED_PAD src0_sel:DWORD src1_sel:WORD_0
	v_or_b32_e32 v76, v72, v26
	v_mul_hi_i32_i24_e32 v69, 0x2c0000, v68
	v_mul_i32_i24_e32 v68, 0x2c0000, v68
	v_mad_i64_i32 v[70:71], s[16:17], v71, s12, v[20:21]
	v_ashrrev_i32_e32 v75, 31, v74
	v_or_b32_e32 v78, 4, v76
	v_or_b32_e32 v80, 8, v76
	v_or_b32_e32 v82, 12, v76
	v_or_b32_e32 v84, 16, v76
	v_or_b32_e32 v86, 20, v76
	v_or_b32_e32 v88, 24, v76
	v_or_b32_e32 v90, 28, v76
	v_or_b32_e32 v92, 32, v76
	v_or_b32_e32 v94, 36, v76
	v_lshl_add_u64 v[68:69], s[6:7], 0, v[68:69]
	v_ashrrev_i32_e32 v73, 31, v72
	v_ashrrev_i32_e32 v77, 31, v76
	v_or_b32_e32 v96, 40, v76
	v_or_b32_e32 v98, 44, v76
	v_or_b32_e32 v100, 48, v76
	v_or_b32_e32 v102, 52, v76
	v_or_b32_e32 v104, 56, v76
	v_or_b32_e32 v106, 60, v76
	v_or_b32_e32 v108, v74, v27
	v_or_b32_e32 v109, v74, v29
	v_or_b32_e32 v110, v74, v30
	v_or_b32_e32 v111, v74, v31
	v_lshl_add_u64 v[70:71], v[74:75], 2, v[70:71]
	v_ashrrev_i32_e32 v79, 31, v78
	v_ashrrev_i32_e32 v81, 31, v80
	v_ashrrev_i32_e32 v83, 31, v82
	v_ashrrev_i32_e32 v85, 31, v84
	v_ashrrev_i32_e32 v87, 31, v86
	v_ashrrev_i32_e32 v89, 31, v88
	v_ashrrev_i32_e32 v91, 31, v90
	v_ashrrev_i32_e32 v93, 31, v92
	v_ashrrev_i32_e32 v95, 31, v94
	v_lshl_add_u64 v[68:69], v[68:69], 0, v[72:73]
	v_lshlrev_b64 v[72:73], 12, v[76:77]
	v_ashrrev_i32_e32 v97, 31, v96
	v_ashrrev_i32_e32 v99, 31, v98
	v_ashrrev_i32_e32 v101, 31, v100
	v_ashrrev_i32_e32 v103, 31, v102
	v_ashrrev_i32_e32 v105, 31, v104
	v_ashrrev_i32_e32 v107, 31, v106
	v_mul_i32_i24_e32 v74, 0xb00, v108
	v_mul_i32_i24_e32 v76, 0xb00, v109
	v_mul_i32_i24_e32 v108, 0xb00, v110
	v_mul_i32_i24_e32 v110, 0xb00, v111
	v_lshl_add_u64 v[70:71], v[70:71], 0, v[22:23]
	v_lshlrev_b64 v[78:79], 12, v[78:79]
	v_lshlrev_b64 v[80:81], 12, v[80:81]
	v_lshlrev_b64 v[82:83], 12, v[82:83]
	v_lshlrev_b64 v[84:85], 12, v[84:85]
	v_lshlrev_b64 v[86:87], 12, v[86:87]
	v_lshlrev_b64 v[88:89], 12, v[88:89]
	v_lshlrev_b64 v[90:91], 12, v[90:91]
	v_lshlrev_b64 v[92:93], 12, v[92:93]
	v_lshlrev_b64 v[94:95], 12, v[94:95]
	v_lshl_add_u64 v[68:69], v[68:69], 0, v[18:19]
	v_lshlrev_b64 v[96:97], 12, v[96:97]
	v_lshlrev_b64 v[98:99], 12, v[98:99]
	v_lshlrev_b64 v[100:101], 12, v[100:101]
	v_lshlrev_b64 v[102:103], 12, v[102:103]
	v_lshlrev_b64 v[104:105], 12, v[104:105]
	v_lshlrev_b64 v[106:107], 12, v[106:107]
	v_ashrrev_i32_e32 v75, 31, v74
	v_ashrrev_i32_e32 v77, 31, v76
	v_ashrrev_i32_e32 v109, 31, v108
	v_ashrrev_i32_e32 v111, 31, v110
	v_lshl_add_u64 v[112:113], v[70:71], 0, v[72:73]
	v_lshl_add_u64 v[114:115], v[70:71], 0, v[78:79]
	v_lshl_add_u64 v[116:117], v[70:71], 0, v[80:81]
	v_lshl_add_u64 v[118:119], v[70:71], 0, v[82:83]
	v_lshl_add_u64 v[120:121], v[70:71], 0, v[84:85]
	v_lshl_add_u64 v[122:123], v[70:71], 0, v[86:87]
	v_lshl_add_u64 v[124:125], v[70:71], 0, v[88:89]
	v_lshl_add_u64 v[126:127], v[70:71], 0, v[90:91]
	v_lshl_add_u64 v[128:129], v[70:71], 0, v[92:93]
	v_lshl_add_u64 v[130:131], v[70:71], 0, v[94:95]
	v_lshl_add_u64 v[132:133], v[70:71], 0, v[96:97]
	v_lshl_add_u64 v[134:135], v[70:71], 0, v[98:99]
	v_lshl_add_u64 v[136:137], v[70:71], 0, v[100:101]
	v_lshl_add_u64 v[140:141], v[70:71], 0, v[102:103]
	v_lshl_add_u64 v[142:143], v[70:71], 0, v[104:105]
	v_lshl_add_u64 v[144:145], v[70:71], 0, v[106:107]
	v_lshl_add_u64 v[146:147], v[68:69], 0, v[74:75]
	v_lshl_add_u64 v[148:149], v[68:69], 0, v[76:77]
	v_lshl_add_u64 v[150:151], v[68:69], 0, v[108:109]
	v_lshl_add_u64 v[152:153], v[68:69], 0, v[110:111]
	global_load_dwordx4 v[68:71], v[112:113], off nt
	global_load_dwordx4 v[72:75], v[114:115], off nt
	global_load_dwordx4 v[76:79], v[116:117], off nt
	global_load_dwordx4 v[80:83], v[118:119], off nt
	global_load_dwordx4 v[84:87], v[120:121], off nt
	global_load_dwordx4 v[88:91], v[122:123], off nt
	global_load_dwordx4 v[92:95], v[124:125], off nt
	global_load_dwordx4 v[96:99], v[126:127], off nt
	global_load_dwordx4 v[100:103], v[128:129], off nt
	global_load_dwordx4 v[104:107], v[130:131], off nt
	global_load_dwordx4 v[108:111], v[132:133], off nt
	global_load_dwordx4 v[112:115], v[134:135], off nt
	global_load_dwordx4 v[116:119], v[136:137], off nt
	global_load_dwordx4 v[120:123], v[140:141], off nt
	global_load_dwordx4 v[124:127], v[142:143], off nt
	global_load_dwordx4 v[128:131], v[144:145], off nt
	s_waitcnt vmcnt(15)
	ds_write2_b32 v32, v68, v69 offset1:1
	ds_write2_b32 v32, v70, v71 offset0:2 offset1:3
	s_waitcnt vmcnt(14)
	ds_write2_b32 v33, v72, v73 offset1:1
	ds_write2_b32 v34, v74, v75 offset1:1
	s_waitcnt vmcnt(13)
	ds_write2_b32 v35, v76, v77 offset1:1
	ds_write2_b32 v36, v78, v79 offset1:1
	s_waitcnt vmcnt(12)
	ds_write2_b32 v37, v80, v81 offset1:1
	ds_write2_b32 v38, v82, v83 offset1:1
	s_waitcnt vmcnt(11)
	ds_write2_b32 v39, v84, v85 offset1:1
	ds_write2_b32 v40, v86, v87 offset1:1
	s_waitcnt vmcnt(10)
	ds_write2_b32 v41, v88, v89 offset1:1
	ds_write2_b32 v42, v90, v91 offset1:1
	s_waitcnt vmcnt(9)
	ds_write2_b32 v43, v92, v93 offset1:1
	ds_write2_b32 v44, v94, v95 offset1:1
	s_waitcnt vmcnt(8)
	ds_write2_b32 v45, v96, v97 offset1:1
	ds_write2_b32 v46, v98, v99 offset1:1
	s_waitcnt vmcnt(7)
	ds_write2_b32 v47, v100, v101 offset1:1
	ds_write2_b32 v48, v102, v103 offset1:1
	s_waitcnt vmcnt(6)
	ds_write2_b32 v49, v104, v105 offset1:1
	ds_write2_b32 v50, v106, v107 offset1:1
	s_waitcnt vmcnt(5)
	ds_write2_b32 v51, v108, v109 offset1:1
	ds_write2_b32 v52, v110, v111 offset1:1
	s_waitcnt vmcnt(4)
	ds_write2_b32 v53, v112, v113 offset1:1
	ds_write2_b32 v54, v114, v115 offset1:1
	s_waitcnt vmcnt(3)
	ds_write2_b32 v55, v116, v117 offset1:1
	ds_write2_b32 v56, v118, v119 offset1:1
	s_waitcnt vmcnt(2)
	ds_write2_b32 v57, v120, v121 offset1:1
	ds_write2_b32 v58, v122, v123 offset1:1
	s_waitcnt vmcnt(1)
	ds_write2_b32 v59, v124, v125 offset1:1
	ds_write2_b32 v60, v126, v127 offset1:1
	s_waitcnt vmcnt(0)
	ds_write2_b32 v61, v128, v129 offset1:1
	ds_write2_b32 v62, v130, v131 offset1:1
	s_waitcnt lgkmcnt(0)
	ds_read2_b32 v[68:69], v28 offset1:16
	ds_read2_b32 v[70:71], v28 offset0:65 offset1:81
	ds_read2_b32 v[72:73], v28 offset0:130 offset1:146
	ds_read2_b32 v[74:75], v28 offset0:195 offset1:211
	ds_read2_b32 v[76:77], v65 offset0:4 offset1:20
	ds_read2_b32 v[78:79], v65 offset0:69 offset1:85
	ds_read2_b32 v[80:81], v65 offset0:134 offset1:150
	ds_read2_b32 v[82:83], v65 offset0:199 offset1:215
	ds_read2_b32 v[84:85], v66 offset0:8 offset1:24
	ds_read2_b32 v[86:87], v66 offset0:73 offset1:89
	ds_read2_b32 v[88:89], v66 offset0:138 offset1:154
	ds_read2_b32 v[90:91], v66 offset0:203 offset1:219
	ds_read2_b32 v[92:93], v67 offset0:12 offset1:28
	ds_read2_b32 v[94:95], v67 offset0:77 offset1:93
	ds_read2_b32 v[96:97], v67 offset0:142 offset1:158
	ds_read2_b32 v[98:99], v67 offset0:207 offset1:223
	ds_read2_b32 v[100:101], v28 offset0:32 offset1:48
	ds_read2_b32 v[102:103], v28 offset0:97 offset1:113
	ds_read2_b32 v[104:105], v28 offset0:162 offset1:178
	ds_read2_b32 v[106:107], v28 offset0:227 offset1:243
	ds_read2_b32 v[108:109], v65 offset0:36 offset1:52
	ds_read2_b32 v[110:111], v65 offset0:101 offset1:117
	ds_read2_b32 v[112:113], v65 offset0:166 offset1:182
	ds_read2_b32 v[114:115], v65 offset0:231 offset1:247
	ds_read2_b32 v[116:117], v66 offset0:40 offset1:56
	ds_read2_b32 v[118:119], v66 offset0:105 offset1:121
	ds_read2_b32 v[120:121], v66 offset0:170 offset1:186
	ds_read2_b32 v[122:123], v66 offset0:235 offset1:251
	ds_read2_b32 v[124:125], v67 offset0:44 offset1:60
	ds_read2_b32 v[126:127], v67 offset0:109 offset1:125
	ds_read2_b32 v[128:129], v67 offset0:174 offset1:190
	ds_read2_b32 v[130:131], v67 offset0:239 offset1:255
	s_waitcnt lgkmcnt(14)
	v_mul_f32_e32 v68, 0x43800000, v68
	v_mul_f32_e32 v70, 0x43800000, v70
	v_mul_f32_e32 v76, 0x43800000, v76
	v_mul_f32_e32 v78, 0x43800000, v78
	v_mul_f32_e32 v84, 0x43800000, v84
	v_mul_f32_e32 v86, 0x43800000, v86
	v_mul_f32_e32 v92, 0x43800000, v92
	v_mul_f32_e32 v94, 0x43800000, v94
	v_mov_b32_e32 v2, 0
	v_mov_b32_e32 v3, 0
	v_mov_b32_e32 v4, 0
	v_mov_b32_e32 v5, 0
	v_mul_f32_e32 v69, 0x43800000, v69
	v_mul_f32_e32 v71, 0x43800000, v71
	v_mul_f32_e32 v77, 0x43800000, v77
	v_mul_f32_e32 v79, 0x43800000, v79
	v_mul_f32_e32 v85, 0x43800000, v85
	v_mul_f32_e32 v87, 0x43800000, v87
	v_mul_f32_e32 v93, 0x43800000, v93
	v_mul_f32_e32 v95, 0x43800000, v95
	v_med3_f32 v68, v68, s13, v63
	v_med3_f32 v70, v70, s13, v63
	v_med3_f32 v76, v76, s13, v63
	v_med3_f32 v78, v78, s13, v63
	v_med3_f32 v84, v84, s13, v63
	v_med3_f32 v86, v86, s13, v63
	v_med3_f32 v92, v92, s13, v63
	v_med3_f32 v94, v94, s13, v63
	v_mov_b32_e32 v6, 0
	v_mov_b32_e32 v7, 0
	v_mov_b32_e32 v8, 0
	v_mov_b32_e32 v9, 0
	v_mul_f32_e32 v100, 0x43800000, v100
	v_mul_f32_e32 v102, 0x43800000, v102
	s_waitcnt lgkmcnt(11)
	v_mul_f32_e32 v108, 0x43800000, v108
	s_waitcnt lgkmcnt(10)
	v_mul_f32_e32 v110, 0x43800000, v110
	s_waitcnt lgkmcnt(7)
	v_mul_f32_e32 v116, 0x43800000, v116
	s_waitcnt lgkmcnt(6)
	v_mul_f32_e32 v118, 0x43800000, v118
	s_waitcnt lgkmcnt(3)
	v_mul_f32_e32 v124, 0x43800000, v124
	s_waitcnt lgkmcnt(2)
	v_mul_f32_e32 v126, 0x43800000, v126
	v_med3_f32 v69, v69, s13, v63
	v_med3_f32 v71, v71, s13, v63
	v_med3_f32 v77, v77, s13, v63
	v_med3_f32 v79, v79, s13, v63
	v_med3_f32 v85, v85, s13, v63
	v_med3_f32 v87, v87, s13, v63
	v_med3_f32 v93, v93, s13, v63
	v_med3_f32 v95, v95, s13, v63
	v_cvt_pk_fp8_f32 v2, v68, v70
	v_cvt_pk_fp8_f32 v3, v76, v78
	v_cvt_pk_fp8_f32 v4, v84, v86
	v_cvt_pk_fp8_f32 v5, v92, v94
	v_mov_b32_e32 v10, 0
	v_mov_b32_e32 v11, 0
	v_mov_b32_e32 v12, 0
	v_mov_b32_e32 v13, 0
	v_mul_f32_e32 v101, 0x43800000, v101
	v_mul_f32_e32 v103, 0x43800000, v103
	v_mul_f32_e32 v109, 0x43800000, v109
	v_mul_f32_e32 v111, 0x43800000, v111
	v_mul_f32_e32 v117, 0x43800000, v117
	v_mul_f32_e32 v119, 0x43800000, v119
	v_mul_f32_e32 v125, 0x43800000, v125
	v_mul_f32_e32 v127, 0x43800000, v127
	v_med3_f32 v100, v100, s13, v63
	v_med3_f32 v102, v102, s13, v63
	v_med3_f32 v108, v108, s13, v63
	v_med3_f32 v110, v110, s13, v63
	v_med3_f32 v116, v116, s13, v63
	v_med3_f32 v118, v118, s13, v63
	v_med3_f32 v124, v124, s13, v63
	v_med3_f32 v126, v126, s13, v63
	v_cvt_pk_fp8_f32 v6, v69, v71
	v_cvt_pk_fp8_f32 v7, v77, v79
	v_cvt_pk_fp8_f32 v8, v85, v87
	v_cvt_pk_fp8_f32 v9, v93, v95
	v_mov_b32_e32 v14, 0
	v_mov_b32_e32 v15, 0
	v_mov_b32_e32 v16, 0
	v_mov_b32_e32 v17, 0
	v_mul_f32_e32 v72, 0x43800000, v72
	v_mul_f32_e32 v74, 0x43800000, v74
	v_mul_f32_e32 v80, 0x43800000, v80
	v_mul_f32_e32 v82, 0x43800000, v82
	v_mul_f32_e32 v88, 0x43800000, v88
	v_mul_f32_e32 v90, 0x43800000, v90
	v_mul_f32_e32 v96, 0x43800000, v96
	v_mul_f32_e32 v98, 0x43800000, v98
	v_med3_f32 v101, v101, s13, v63
	v_med3_f32 v103, v103, s13, v63
	v_med3_f32 v109, v109, s13, v63
	v_med3_f32 v111, v111, s13, v63
	v_med3_f32 v117, v117, s13, v63
	v_med3_f32 v119, v119, s13, v63
	v_med3_f32 v125, v125, s13, v63
	v_med3_f32 v127, v127, s13, v63
	v_cvt_pk_fp8_f32 v10, v100, v102
	v_cvt_pk_fp8_f32 v11, v108, v110
	v_cvt_pk_fp8_f32 v12, v116, v118
	v_cvt_pk_fp8_f32 v13, v124, v126
	v_mul_f32_e32 v73, 0x43800000, v73
	v_mul_f32_e32 v75, 0x43800000, v75
	v_mul_f32_e32 v81, 0x43800000, v81
	v_mul_f32_e32 v83, 0x43800000, v83
	v_mul_f32_e32 v89, 0x43800000, v89
	v_mul_f32_e32 v91, 0x43800000, v91
	v_mul_f32_e32 v97, 0x43800000, v97
	v_mul_f32_e32 v99, 0x43800000, v99
	v_med3_f32 v72, v72, s13, v63
	v_med3_f32 v74, v74, s13, v63
	v_med3_f32 v80, v80, s13, v63
	v_med3_f32 v82, v82, s13, v63
	v_med3_f32 v88, v88, s13, v63
	v_med3_f32 v90, v90, s13, v63
	v_med3_f32 v96, v96, s13, v63
	v_med3_f32 v98, v98, s13, v63
	v_cvt_pk_fp8_f32 v14, v101, v103
	v_cvt_pk_fp8_f32 v15, v109, v111
	v_cvt_pk_fp8_f32 v16, v117, v119
	v_cvt_pk_fp8_f32 v17, v125, v127
	v_mul_f32_e32 v104, 0x43800000, v104
	v_mul_f32_e32 v106, 0x43800000, v106
	v_mul_f32_e32 v112, 0x43800000, v112
	v_mul_f32_e32 v114, 0x43800000, v114
	v_mul_f32_e32 v120, 0x43800000, v120
	v_mul_f32_e32 v122, 0x43800000, v122
	s_waitcnt lgkmcnt(1)
	v_mul_f32_e32 v128, 0x43800000, v128
	s_waitcnt lgkmcnt(0)
	v_mul_f32_e32 v130, 0x43800000, v130
	v_med3_f32 v73, v73, s13, v63
	v_med3_f32 v75, v75, s13, v63
	v_med3_f32 v81, v81, s13, v63
	v_med3_f32 v83, v83, s13, v63
	v_med3_f32 v89, v89, s13, v63
	v_med3_f32 v91, v91, s13, v63
	v_med3_f32 v97, v97, s13, v63
	v_med3_f32 v99, v99, s13, v63
	v_cvt_pk_fp8_f32 v2, v72, v74 op_sel:[0,0,1]
	v_cvt_pk_fp8_f32 v3, v80, v82 op_sel:[0,0,1]
	v_cvt_pk_fp8_f32 v4, v88, v90 op_sel:[0,0,1]
	v_cvt_pk_fp8_f32 v5, v96, v98 op_sel:[0,0,1]
	v_mul_f32_e32 v105, 0x43800000, v105
	v_mul_f32_e32 v107, 0x43800000, v107
	v_mul_f32_e32 v113, 0x43800000, v113
	v_mul_f32_e32 v115, 0x43800000, v115
	v_mul_f32_e32 v121, 0x43800000, v121
	v_mul_f32_e32 v123, 0x43800000, v123
	v_mul_f32_e32 v129, 0x43800000, v129
	v_mul_f32_e32 v131, 0x43800000, v131
	v_med3_f32 v104, v104, s13, v63
	v_med3_f32 v106, v106, s13, v63
	v_med3_f32 v112, v112, s13, v63
	v_med3_f32 v114, v114, s13, v63
	v_med3_f32 v120, v120, s13, v63
	v_med3_f32 v122, v122, s13, v63
	v_med3_f32 v128, v128, s13, v63
	v_med3_f32 v130, v130, s13, v63
	v_cvt_pk_fp8_f32 v6, v73, v75 op_sel:[0,0,1]
	v_cvt_pk_fp8_f32 v7, v81, v83 op_sel:[0,0,1]
	v_cvt_pk_fp8_f32 v8, v89, v91 op_sel:[0,0,1]
	v_cvt_pk_fp8_f32 v9, v97, v99 op_sel:[0,0,1]
	v_med3_f32 v105, v105, s13, v63
	v_med3_f32 v107, v107, s13, v63
	v_med3_f32 v113, v113, s13, v63
	v_med3_f32 v115, v115, s13, v63
	v_med3_f32 v121, v121, s13, v63
	v_med3_f32 v123, v123, s13, v63
	v_med3_f32 v129, v129, s13, v63
	v_med3_f32 v131, v131, s13, v63
	v_cvt_pk_fp8_f32 v10, v104, v106 op_sel:[0,0,1]
	v_cvt_pk_fp8_f32 v11, v112, v114 op_sel:[0,0,1]
	v_cvt_pk_fp8_f32 v12, v120, v122 op_sel:[0,0,1]
	v_cvt_pk_fp8_f32 v13, v128, v130 op_sel:[0,0,1]
	v_cvt_pk_fp8_f32 v14, v105, v107 op_sel:[0,0,1]
	v_cvt_pk_fp8_f32 v15, v113, v115 op_sel:[0,0,1]
	v_cvt_pk_fp8_f32 v16, v121, v123 op_sel:[0,0,1]
	v_cvt_pk_fp8_f32 v17, v129, v131 op_sel:[0,0,1]
	global_store_dwordx4 v[146:147], v[2:5], off
	global_store_dwordx4 v[148:149], v[6:9], off
	global_store_dwordx4 v[150:151], v[10:13], off
	global_store_dwordx4 v[152:153], v[14:17], off
	v_add_u32_e32 v1, s10, v1
	s_waitcnt lgkmcnt(0)
	v_cmp_lt_i32_e32 vcc, s14, v1
	s_or_b64 s[8:9], vcc, s[8:9]
	s_andn2_b64 exec, exec, s[8:9]
	s_cbranch_execnz .LBB0_2378
